# speedup vs baseline: 1.0024x; 1.0024x over previous
.Lattn_after_rdv:
	s_cbranch_scc1 .Lattn_skip_tile
	ds_read_b128 v[46:49], v114
	ds_read_b128 v[42:45], v114 offset:2048
	ds_read_b128 v[38:41], v114 offset:4096
	ds_read_b128 v[34:37], v114 offset:6144
	ds_read_b128 v[102:105], v115
	ds_read_b128 v[106:109], v115 offset:2048
	ds_read_b128 v[110:113], v115 offset:4096
	ds_read_b128 v[76:79], v115 offset:6144
	s_cmp_lt_i32 s64, s79
	s_cbranch_scc1 .Lattn_do_dma
.Lattn_no_dma:
	s_add_i32 s48, s66, s64
	s_cmp_lg_u32 s48, 1
	s_waitcnt lgkmcnt(7)
	v_mfma_f32_16x16x32_f16 v[46:49], v[46:49], v[6:9], v[30:33]
	s_waitcnt lgkmcnt(6)
	v_mfma_f32_16x16x32_f16 v[42:45], v[42:45], v[6:9], v[30:33]
	s_waitcnt lgkmcnt(5)
	v_mfma_f32_16x16x32_f16 v[38:41], v[38:41], v[6:9], v[30:33]
	s_waitcnt lgkmcnt(4)
	v_mfma_f32_16x16x32_f16 v[34:37], v[34:37], v[6:9], v[30:33]
	s_waitcnt lgkmcnt(3)
	v_mfma_f32_16x16x32_f16 v[46:49], v[102:105], v[2:5], v[46:49]
	s_waitcnt lgkmcnt(2)
	v_mfma_f32_16x16x32_f16 v[42:45], v[106:109], v[2:5], v[42:45]
	s_waitcnt lgkmcnt(1)
	v_mfma_f32_16x16x32_f16 v[38:41], v[110:113], v[2:5], v[38:41]
	s_waitcnt lgkmcnt(0)
	v_mfma_f32_16x16x32_f16 v[34:37], v[76:79], v[2:5], v[34:37]
	s_cbranch_scc1 .LBB2_12
	s_nop 0
	v_cndmask_b32_e64 v69, v46, v100, s[2:3]
	v_cndmask_b32_e64 v46, v69, v46, s[4:5]
	v_cndmask_b32_e64 v47, v100, v47, s[4:5]
	v_cndmask_b32_e64 v48, v48, v100, s[6:7]
	v_cndmask_b32_e64 v49, v49, v100, s[8:9]
	v_cndmask_b32_e64 v42, v42, v100, s[10:11]
	v_cndmask_b32_e64 v43, v43, v100, s[12:13]
	v_cndmask_b32_e64 v44, v44, v100, s[14:15]
	v_cndmask_b32_e64 v45, v45, v100, s[16:17]
	v_cndmask_b32_e64 v38, v38, v100, s[18:19]
	v_cndmask_b32_e64 v39, v39, v100, s[20:21]
	v_cndmask_b32_e64 v40, v40, v100, s[22:23]
	v_cndmask_b32_e64 v41, v41, v100, s[24:25]
	v_cndmask_b32_e64 v34, v34, v100, s[26:27]
	v_cndmask_b32_e64 v35, v35, v100, s[28:29]
	v_cndmask_b32_e64 v36, v36, v100, s[30:31]
	v_cndmask_b32_e64 v37, v37, v100, s[34:35]
.LBB2_12:
	s_and_b64 vcc, exec, s[38:39]
	v_max3_f32 v69, v46, v47, v48
	s_nop 1
	v_max3_f32 v71, v49, v42, v43
	v_max3_f32 v69, v69, v44, v45
	v_max3_f32 v71, v71, v38, v39
	v_max3_f32 v69, v69, v40, v41
	v_max3_f32 v71, v71, v34, v35
	v_max3_f32 v69, v69, v36, v37
	v_max_f32_e32 v69, v69, v71
	s_cbranch_vccnz .Lattn_first_tile
	v_cmp_lt_f32_e32 vcc, s58, v69
	s_nop 1
	s_cbranch_vccz .LBB2_5
	v_mov_b32_e32 v71, v69
	s_nop 1
	v_permlane16_swap_b32_e32 v69, v71
	v_max_f32_e32 v69, v69, v71
	v_mov_b32_e32 v71, v69
	s_nop 1
	v_permlane32_swap_b32_e32 v69, v71
	v_max_f32_e32 v69, v69, v71
	v_max_f32_e32 v71, v69, v69
	v_max_f32_e32 v80, 0, v71
	s_branch .Lattn_rescale
